# prep_all: non-temporal policy on all read-once input loads (weights, proj, bias), on top of attn older-wave priority + reduce_slabs rewrite
# speedup vs baseline: 1.0240x; 1.0022x over previous
.LBB0_8:
	v_add_co_u32_e32 v8, vcc, 0xffff9000, v4
	s_add_i32 s33, s33, 32
	s_nop 0
	v_addc_co_u32_e32 v9, vcc, -1, v5, vcc
	v_add_co_u32_e32 v10, vcc, 0xffffa000, v4
	s_cmpk_gt_u32 s33, 0xfb
	s_nop 0
	v_addc_co_u32_e32 v11, vcc, -1, v5, vcc
	v_add_co_u32_e32 v12, vcc, 0xffffb000, v4
	global_load_dword v14, v[8:9], off offset:-3072 nt
	global_load_dword v16, v[8:9], off offset:-2048 nt
	global_load_dword v15, v[8:9], off offset:-1024 nt
	global_load_dword v17, v[8:9], off nt
	global_load_dword v18, v[10:11], off offset:-3072 nt
	global_load_dword v20, v[10:11], off offset:-2048 nt
	global_load_dword v19, v[10:11], off offset:-1024 nt
	global_load_dword v21, v[10:11], off nt
	v_addc_co_u32_e32 v13, vcc, -1, v5, vcc
	v_add_co_u32_e32 v8, vcc, 0xffffc000, v4
	s_waitcnt vmcnt(5)
	v_pk_add_f32 v[2:3], v[2:3], v[14:15]
	v_addc_co_u32_e32 v9, vcc, -1, v5, vcc
	v_add_co_u32_e32 v10, vcc, 0xffffd000, v4
	global_load_dword v22, v[12:13], off offset:-3072 nt
	global_load_dword v24, v[12:13], off offset:-2048 nt
	global_load_dword v23, v[12:13], off offset:-1024 nt
	global_load_dword v25, v[12:13], off nt
	global_load_dword v26, v[8:9], off offset:-3072 nt
	global_load_dword v28, v[8:9], off offset:-2048 nt
	global_load_dword v27, v[8:9], off offset:-1024 nt
	global_load_dword v29, v[8:9], off nt
	v_addc_co_u32_e32 v11, vcc, -1, v5, vcc
	v_add_co_u32_e32 v8, vcc, 0xffffe000, v4
	s_waitcnt vmcnt(12)
	v_pk_add_f32 v[6:7], v[6:7], v[16:17]
	v_addc_co_u32_e32 v9, vcc, -1, v5, vcc
	v_add_co_u32_e32 v12, vcc, 0xfffff000, v4
	global_load_dword v30, v[10:11], off offset:-3072 nt
	global_load_dword v32, v[10:11], off offset:-2048 nt
	global_load_dword v31, v[10:11], off offset:-1024 nt
	global_load_dword v33, v[10:11], off nt
	global_load_dword v34, v[8:9], off offset:-3072 nt
	global_load_dword v36, v[8:9], off offset:-2048 nt
	global_load_dword v35, v[8:9], off offset:-1024 nt
	global_load_dword v37, v[8:9], off nt
	v_addc_co_u32_e32 v13, vcc, -1, v5, vcc
	global_load_dword v8, v[12:13], off offset:-3072 nt
	global_load_dword v10, v[12:13], off offset:-2048 nt
	global_load_dword v9, v[12:13], off offset:-1024 nt
	global_load_dword v11, v[4:5], off offset:-4096 nt
	global_load_dword v38, v[4:5], off offset:-3072 nt
	global_load_dword v40, v[4:5], off offset:-2048 nt
	global_load_dword v39, v[4:5], off offset:-1024 nt
	global_load_dword v41, v[4:5], off nt
	s_waitcnt vmcnt(25)
	v_pk_add_f32 v[2:3], v[2:3], v[18:19]
	s_waitcnt vmcnt(24)
	v_pk_add_f32 v[6:7], v[6:7], v[20:21]
	v_lshl_add_u64 v[4:5], v[4:5], 0, s[30:31]
	s_waitcnt vmcnt(21)
	v_pk_add_f32 v[2:3], v[2:3], v[22:23]
	s_waitcnt vmcnt(20)
	v_pk_add_f32 v[6:7], v[6:7], v[24:25]
	s_waitcnt vmcnt(17)
	v_pk_add_f32 v[2:3], v[2:3], v[26:27]
	s_waitcnt vmcnt(16)
	v_pk_add_f32 v[6:7], v[6:7], v[28:29]
	s_waitcnt vmcnt(13)
	v_pk_add_f32 v[2:3], v[2:3], v[30:31]
	s_waitcnt vmcnt(12)
	v_pk_add_f32 v[6:7], v[6:7], v[32:33]
	s_waitcnt vmcnt(9)
	v_pk_add_f32 v[2:3], v[2:3], v[34:35]
	s_waitcnt vmcnt(8)
	v_pk_add_f32 v[6:7], v[6:7], v[36:37]
	s_waitcnt vmcnt(5)
	v_pk_add_f32 v[2:3], v[2:3], v[8:9]
	s_waitcnt vmcnt(4)
	v_pk_add_f32 v[6:7], v[6:7], v[10:11]
	s_waitcnt vmcnt(1)
	v_pk_add_f32 v[2:3], v[2:3], v[38:39]
	s_waitcnt vmcnt(0)
	v_pk_add_f32 v[6:7], v[6:7], v[40:41]
	s_cbranch_scc0 .LBB0_8
	v_pk_add_f32 v[2:3], v[2:3], v[6:7]
	v_mov_b32_e32 v4, s26
	v_mov_b32_e32 v5, s27
	v_add_f32_e32 v1, v2, v3
	v_lshl_or_b32 v2, s3, 8, v0
	v_mov_b32_e32 v3, 0
	v_lshl_add_u64 v[2:3], v[2:3], 2, v[4:5]
	s_mov_b64 s[30:31], 0
	global_store_dword v[2:3], v1, off

.LBB0_12:
	v_add_lshl_u32 v10, v9, s36, 8
	v_add_lshl_u32 v15, v8, s34, 8
	v_add_lshl_u32 v26, v8, s28, 8
	v_or_b32_e32 v16, v1, v10
	v_or_b32_e32 v10, v6, v15
	v_mov_b32_e32 v17, v11
	v_add_lshl_u32 v18, v9, s29, 8
	v_add_lshl_u32 v28, v8, s30, 8
	v_lshl_add_u64 v[24:25], v[10:11], 2, s[26:27]
	v_or_b32_e32 v10, v6, v26
	v_mov_b32_e32 v19, v11
	v_add_lshl_u32 v20, v9, s31, 8
	v_add_lshl_u32 v22, v9, s38, 8
	v_add_lshl_u32 v29, v8, s37, 8
	v_or_b32_e32 v18, v1, v18
	v_lshl_add_u64 v[16:17], v[16:17], 2, s[26:27]
	v_lshl_add_u64 v[26:27], v[10:11], 2, s[26:27]
	v_or_b32_e32 v10, v6, v28
	v_mov_b32_e32 v21, v11
	v_mov_b32_e32 v23, v11
	v_or_b32_e32 v20, v1, v20
	v_or_b32_e32 v22, v1, v22
	v_lshl_add_u64 v[18:19], v[18:19], 2, s[26:27]
	global_load_dword v15, v[24:25], off nt
	global_load_dword v28, v[16:17], off nt
	global_load_dword v30, v[26:27], off nt
	global_load_dword v31, v[18:19], off nt
	v_lshl_add_u64 v[16:17], v[10:11], 2, s[26:27]
	v_or_b32_e32 v10, v6, v29
	v_lshl_add_u64 v[20:21], v[20:21], 2, s[26:27]
	v_lshl_add_u64 v[22:23], v[22:23], 2, s[26:27]
	v_lshl_add_u64 v[18:19], v[10:11], 2, s[26:27]
	global_load_dword v10, v[16:17], off nt
	global_load_dword v24, v[20:21], off nt
	global_load_dword v25, v[18:19], off nt
	global_load_dword v26, v[22:23], off nt
	v_add_u32_e32 v12, -4, v12
	v_cmp_eq_u32_e32 vcc, 0, v12
	v_add_u32_e32 v9, 32, v9
	v_add_u32_e32 v8, 32, v8
	s_or_b64 s[18:19], vcc, s[18:19]
	s_waitcnt vmcnt(7)
	ds_write_b32 v7, v15
	s_waitcnt vmcnt(6)
	ds_write_b32 v7, v28 offset:1040
	s_waitcnt vmcnt(5)
	ds_write_b32 v7, v30 offset:2080
	s_waitcnt vmcnt(4)
	ds_write_b32 v7, v31 offset:3120
	s_waitcnt vmcnt(3)
	ds_write_b32 v7, v10 offset:4160
	s_waitcnt vmcnt(2)
	ds_write_b32 v7, v24 offset:5200
	s_waitcnt vmcnt(1)
	ds_write_b32 v7, v25 offset:6240
	s_waitcnt vmcnt(0)
	ds_write_b32 v7, v26 offset:7280
	v_add_u32_e32 v7, 0x2080, v7
	s_andn2_b64 exec, exec, s[18:19]
	s_cbranch_execnz .LBB0_12
	s_or_b64 exec, exec, s[18:19]
	v_mov_b32_e32 v12, 0
	v_cmp_ne_u32_e64 s[18:19], 0, 0
	s_and_saveexec_b64 s[28:29], s[18:19]
	s_cbranch_execz .LBB0_16
	s_mov_b64 s[30:31], 0
	v_mov_b32_e32 v11, 0
	v_mov_b32_e32 v15, 0
.LBB0_15:
	v_add_lshl_u32 v10, v9, s36, 8
	v_add_lshl_u32 v18, v8, s34, 8
	v_or_b32_e32 v16, v1, v10
	v_or_b32_e32 v10, v6, v18
	v_mov_b32_e32 v17, v11
	v_lshl_add_u64 v[18:19], v[10:11], 2, s[26:27]
	v_lshl_add_u64 v[16:17], v[16:17], 2, s[26:27]
	global_load_dword v10, v[18:19], off nt
	global_load_dword v20, v[16:17], off nt
	v_add_u32_e32 v15, -1, v15
	v_cmp_eq_u32_e32 vcc, 0, v15
	v_add_u32_e32 v9, 8, v9
	v_add_u32_e32 v8, 8, v8
	s_or_b64 s[30:31], vcc, s[30:31]
	s_waitcnt vmcnt(1)
	ds_write_b32 v7, v10
	s_waitcnt vmcnt(0)
	ds_write_b32 v7, v20 offset:1040
	v_add_u32_e32 v7, 0x820, v7
	s_andn2_b64 exec, exec, s[30:31]
	s_cbranch_execnz .LBB0_15

.LBB0_18:
	global_load_dword v11, v[6:7], off nt
	v_add_u32_e32 v8, 4, v8
	v_cmp_lt_u32_e32 vcc, 59, v8
	v_lshl_add_u64 v[6:7], v[6:7], 0, s[26:27]
	s_or_b64 s[28:29], vcc, s[28:29]
	s_waitcnt vmcnt(0)
	ds_write_b32 v9, v11
	v_add_u32_e32 v9, 0x410, v9
	s_andn2_b64 exec, exec, s[28:29]
	s_cbranch_execnz .LBB0_18

.LBB0_31:
	v_and_b32_e32 v2, 0xc00, v13
	v_and_b32_e32 v14, 15, v6
	v_cmp_eq_u32_e32 vcc, s3, v2
	v_and_or_b32 v2, v1, s14, v14
	v_lshlrev_b32_e32 v2, 2, v2
	v_cndmask_b32_e32 v16, v7, v8, vcc
	v_cndmask_b32_e32 v14, v9, v10, vcc
	v_cmp_gt_u32_e32 vcc, s3, v13
	v_add_u32_e32 v6, 4, v6
	v_add_u32_e32 v1, 0x1000, v1
	v_cndmask_b32_e32 v15, v14, v11, vcc
	v_cndmask_b32_e32 v14, v16, v12, vcc
	v_lshl_add_u64 v[14:15], v[14:15], 0, v[2:3]
	global_load_dword v2, v[14:15], off nt
	v_add_u32_e32 v14, 0x100, v13
	v_cmp_lt_u32_e32 vcc, s15, v13
	s_or_b64 s[18:19], vcc, s[18:19]
	v_mov_b32_e32 v13, v14
	s_waitcnt vmcnt(0)
	global_store_dword v[4:5], v2, off
	v_lshl_add_u64 v[4:5], v[4:5], 0, s[12:13]
	s_andn2_b64 exec, exec, s[18:19]
	s_cbranch_execnz .LBB0_31
	s_or_b64 exec, exec, s[18:19]

.LBB0_34:
	s_andn2_b64 vcc, exec, s[28:29]
	s_cbranch_vccnz .LBB0_36
	s_lshl_b32 s3, s2, 1
	s_waitcnt lgkmcnt(0)
	s_add_i32 s12, s3, 0xffffd400
	s_mov_b32 s13, 0
	s_lshl_b64 s[14:15], s[12:13], 12
	s_add_u32 s10, s10, s14
	s_addc_u32 s11, s11, s15
	v_lshlrev_b32_e32 v10, 4, v0
	v_mov_b32_e32 v11, 0
	v_lshl_add_u64 v[2:3], s[10:11], 0, v[10:11]
	v_add_co_u32_e32 v12, vcc, 0x1000, v2
	v_lshrrev_b32_e32 v1, 7, v0
	s_nop 0
	v_addc_co_u32_e32 v13, vcc, 0, v3, vcc
	global_load_dwordx4 v[2:5], v10, s[10:11] nt
	global_load_dwordx4 v[6:9], v[12:13], off nt
	v_lshrrev_b32_e32 v12, 1, v0
	v_lshlrev_b32_e32 v13, 9, v0
	v_lshlrev_b32_e32 v14, 12, v1
	v_and_b32_e32 v12, 60, v12
	v_and_b32_e32 v15, 0xe00, v13
	v_or3_b32 v14, v14, v12, v15
	v_mov_b32_e32 v13, v11
	v_or_b32_e32 v12, s12, v1
	v_lshlrev_b64 v[12:13], 11, v[12:13]
	v_lshl_add_u64 v[12:13], s[20:21], 0, v[12:13]
	s_waitcnt vmcnt(1)
	ds_write_b128 v10, v[2:5]
	s_waitcnt vmcnt(0)
	ds_write_b128 v10, v[6:9] offset:4096
	s_waitcnt lgkmcnt(0)
	s_barrier
	ds_read2_b32 v[6:7], v14 offset1:16
	ds_read2_b32 v[2:3], v14 offset0:32 offset1:48
	ds_read2_b32 v[8:9], v14 offset0:64 offset1:80
	ds_read2_b32 v[4:5], v14 offset0:96 offset1:112
	v_and_b32_e32 v10, 0x7f0, v10
	v_lshl_add_u64 v[10:11], v[12:13], 0, v[10:11]
	v_add_co_u32_e32 v10, vcc, 0x600000, v10
	s_waitcnt lgkmcnt(0)
	v_cvt_pk_f16_f32 v5, v4, v5
	v_cvt_pk_f16_f32 v4, v8, v9
	v_cvt_pk_f16_f32 v3, v2, v3
	v_cvt_pk_f16_f32 v2, v6, v7
	v_addc_co_u32_e32 v11, vcc, 0, v11, vcc
	global_store_dwordx4 v[10:11], v[2:5], off

.LBB0_37:
	s_andn2_b64 vcc, exec, s[28:29]
	s_cbranch_vccnz .LBB0_39
	s_add_i32 s3, s2, 0xfffff000
	s_waitcnt lgkmcnt(0)
	s_lshl_b32 s11, s2, 8
	s_lshr_b32 s10, s3, 9
	s_and_b32 s12, s11, 0x1ff00
	v_or_b32_e32 v1, s12, v0
	s_cmp_eq_u32 s10, 1
	s_cselect_b32 s6, s6, s8
	s_cselect_b32 s7, s7, s9
	s_cmpk_lt_u32 s3, 0x200
	v_lshrrev_b32_e32 v2, 3, v1
	s_cselect_b32 s5, s5, s7
	s_cselect_b32 s4, s4, s6
	v_and_b32_e32 v2, 0x3f0, v2
	s_bfe_u32 s3, s11, 0x4000d
	v_or_b32_e32 v2, s3, v2
	v_lshlrev_b32_e32 v2, 12, v2
	v_mov_b32_e32 v3, 0
	v_lshl_add_u64 v[4:5], s[4:5], 0, v[2:3]
	v_lshlrev_b32_e32 v2, 5, v0
	v_and_b32_e32 v2, 0xfe0, v2
	v_lshl_add_u64 v[10:11], v[4:5], 0, v[2:3]
	global_load_dwordx4 v[2:5], v[10:11], off nt
	global_load_dwordx4 v[6:9], v[10:11], off offset:16 nt
	s_mov_b32 s11, 0
	s_lshl_b64 s[4:5], s[10:11], 21
	s_add_u32 s4, s20, s4
	s_addc_u32 s5, s21, s5
	v_lshlrev_b32_e32 v1, 4, v1
	s_waitcnt vmcnt(1)
	v_cvt_f16_f32_e32 v2, v2
	v_cvt_pk_f16_f32 v10, v3, v4
	s_waitcnt vmcnt(0)
	v_cvt_pk_f16_f32 v4, v5, v6
	v_cvt_f16_f32_e32 v6, v9
	v_cvt_pk_f16_f32 v5, v7, v8
	v_alignbit_b32 v3, v4, v10, 16
	v_alignbit_b32 v4, v5, v4, 16
	v_pack_b32_f16 v2, v2, v10
	v_alignbit_b32 v5, v6, v5, 16
	global_store_dwordx4 v1, v[2:5], s[4:5]
